# attention PV block: V transpose reads double-buffered, first group issued before the softmax, counted lgkmcnt waits (strategy 1+8), on top of best
# speedup vs baseline: 1.1014x; 1.0058x over previous
; #define LAS __attribute__((address_space(3)))
; __device__ __forceinline__ void qkt(f32x16& p0, f32x16& p1, LAS unsigned char* lds  , int r32, int hi, const bf16x8* qr) {
;     p0 = f32x16{}; p1 = f32x16{};
;     const LAS unsigned char* kb[4];
; #pragma unroll
;     for (int dd = 0; dd < 4; ++dd) kb[dd] = lds + K_OFF + KSWZ(r32, (dd * 16 + hi * 8) * 2);
; #pragma unroll
;     for (int d0 = 0; d0 < 8; ++d0) { const LAS unsigned char* a = kb[d0 & 3] + (d0 >> 2) * 128;
;         const bf16x8 b0 = *(const LAS bf16x8*)(a);
;         const bf16x8 b1 = *(const LAS bf16x8*)(a + 32 * 256);
;         p0 = __builtin_amdgcn_mfma_f32_32x32x16_bf16(b0, qr[d0], p0, 0, 0, 0);
;         p1 = __builtin_amdgcn_mfma_f32_32x32x16_bf16(b1, qr[d0], p1, 0, 0, 0); }
; #pragma unroll
;     for (int e = 0; e < 4; ++e) { const LAS unsigned char* a = lds + P_OFF + KPSWZ(r32, (e * 2 + hi) * 16);
;         const bf16x8 b0 = *(const LAS bf16x8*)(a);
;         const bf16x8 b1 = *(const LAS bf16x8*)(a + 32 * 128);
;         p0 = __builtin_amdgcn_mfma_f32_32x32x16_bf16(b0, qr[8 + e], p0, 0, 0, 0);
;         p1 = __builtin_amdgcn_mfma_f32_32x32x16_bf16(b1, qr[8 + e], p1, 0, 0, 0); }
; }
; __device__ __forceinline__ void pv_tile(f32x16* o, int vb0  , bf16x8 pa0, bf16x8 pa1, bf16x8 pa2, bf16x8 pa3) {
; __device__ __forceinline__ void attn_unit(LAS unsigned char* lds, int b, int h, int qb, const bf16* Q  , const bf16* KV  , const bf16* KPE  ,
;                                           const float* ROPE  , bf16* O  , const int wave_) {
;     ...
;     for (int t = 0; t < NT; ++t) {
;         asm volatile("s_waitcnt vmcnt(5)" ::: "memory"); __builtin_amdgcn_s_barrier();
;         { const int tn = (t + 2 < NT) ? t + 2 : NT - 1; AISSUE(tn, bl); }
;         const int kb_ = t * KVBLK;
;         if (kb_ <= qlo + 31) {
;             SBAR(); qkt(p0, p1, lds + bc, r32, hi, qr);
;             if (kb_ + KVBLK - 1 > qlo) mask_tile(p0, p1, qm - kb_);
;             partialSM(p0, p1, m_reg, mn, alpha);
;             if (__any(alpha < 1.f)) { if (hi == 0) al_l[r32] = alpha; LDS_WAIT();
; #pragma unroll
;                 for (int d_ = 0; d_ < 4; ++d_)
; #pragma unroll
;                     for (int r = 0; r < 16; ++r) o[d_][r] *= al_l[crow(r, hi)]; }
;             finishSM(p0, p1, alpha, l_reg, pa0, pa1, pa2, pa3); SBAR();
;             pv_tile(o, vb0 + bc, pa0, pa1, pa2, pa3); }
.LBB0_720:
	s_add_i32 s4, s73, 2
	s_min_u32 s70, s4, s2
	s_lshl_b64 s[4:5], s[70:71], 18
	s_add_u32 s4, s96, s4
	s_addc_u32 s5, s97, s5
	v_lshl_add_u64 v[64:65], v[150:151], 1, s[4:5]
	s_add_i32 s8, s95, s69
	v_lshl_add_u64 v[64:65], v[64:65], 0, s[66:67]
	s_mov_b32 m0, s8
	s_waitcnt vmcnt(5)
	s_barrier
	global_load_lds_dwordx4 v[64:65], off
	v_lshl_add_u64 v[64:65], v[152:153], 1, s[4:5]
	v_lshl_add_u64 v[64:65], v[64:65], 0, s[66:67]
	s_add_i32 m0, s8, 0x2000
	s_lshl_b64 s[6:7], s[70:71], 13
	global_load_lds_dwordx4 v[64:65], off
	v_lshl_add_u64 v[64:65], v[146:147], 1, s[4:5]
	s_add_i32 m0, s8, 0x4000
	s_nop 0
	global_load_lds_dwordx4 v[64:65], off
	v_lshl_add_u64 v[64:65], v[148:149], 1, s[4:5]
	s_add_i32 m0, s8, 0x6000
	s_sub_i32 s4, s94, 63
	global_load_lds_dwordx4 v[64:65], off
	v_lshl_add_u64 v[64:65], v[154:155], 0, s[6:7]
	s_add_i32 m0, s8, 0x8000
	s_cmp_gt_i32 s4, s68
	global_load_lds_dwordx4 v[64:65], off
	s_cbranch_scc1 .LBB0_728
	s_add_i32 s4, s72, 0
	v_add_u32_e32 v216, s4, v160
	v_add_u32_e32 v220, s4, v166
	v_add_u32_e32 v217, v216, v162
	v_add_u32_e32 v218, v216, v163
	v_add_u32_e32 v219, v216, v165
	v_add_u32_e32 v216, v216, v161
	v_add_u32_e32 v221, v220, v168
	v_add_u32_e32 v222, v220, v169
	v_add_u32_e32 v223, v220, v170
	v_add_u32_e32 v220, v220, v167
	ds_read_b128 v[176:179], v216 offset:16384
	ds_read_b128 v[180:183], v216 offset:24576
	ds_read_b128 v[184:187], v217 offset:16384
	ds_read_b128 v[188:191], v217 offset:24576
	ds_read_b128 v[192:195], v218 offset:16384
	ds_read_b128 v[196:199], v218 offset:24576
	ds_read_b128 v[200:203], v219 offset:16384
	ds_read_b128 v[204:207], v219 offset:24576
	s_cmp_le_i32 s94, s33
	ds_read_b128 v[208:211], v216 offset:16512
	ds_read_b128 v[212:215], v216 offset:24704
	s_waitcnt lgkmcnt(8)
	v_mfma_f32_32x32x16_bf16 v[80:95], v[176:179], v[124:127], 0
	v_mfma_f32_32x32x16_bf16 v[64:79], v[180:183], v[124:127], 0
	ds_read_b128 v[176:179], v217 offset:16512
	ds_read_b128 v[180:183], v217 offset:24704
	s_waitcnt lgkmcnt(8)
	v_mfma_f32_32x32x16_bf16 v[80:95], v[184:187], v[100:103], v[80:95]
	v_mfma_f32_32x32x16_bf16 v[64:79], v[188:191], v[100:103], v[64:79]
	ds_read_b128 v[184:187], v218 offset:16512
	ds_read_b128 v[188:191], v218 offset:24704
	s_waitcnt lgkmcnt(8)
	v_mfma_f32_32x32x16_bf16 v[80:95], v[192:195], v[104:107], v[80:95]
	v_mfma_f32_32x32x16_bf16 v[64:79], v[196:199], v[104:107], v[64:79]
	ds_read_b128 v[192:195], v219 offset:16512
	ds_read_b128 v[196:199], v219 offset:24704
	s_waitcnt lgkmcnt(8)
	v_mfma_f32_32x32x16_bf16 v[80:95], v[200:203], v[108:111], v[80:95]
	v_mfma_f32_32x32x16_bf16 v[64:79], v[204:207], v[108:111], v[64:79]
	ds_read_b128 v[200:203], v220 offset:32768
	ds_read_b128 v[204:207], v220 offset:36864
	s_waitcnt lgkmcnt(8)
	v_mfma_f32_32x32x16_bf16 v[80:95], v[208:211], v[112:115], v[80:95]
	v_mfma_f32_32x32x16_bf16 v[64:79], v[212:215], v[112:115], v[64:79]
	ds_read_b128 v[208:211], v221 offset:32768
	ds_read_b128 v[212:215], v221 offset:36864
	s_waitcnt lgkmcnt(8)
	v_mfma_f32_32x32x16_bf16 v[80:95], v[176:179], v[116:119], v[80:95]
	v_mfma_f32_32x32x16_bf16 v[64:79], v[180:183], v[116:119], v[64:79]
	ds_read_b128 v[176:179], v222 offset:32768
	ds_read_b128 v[180:183], v222 offset:36864
	s_waitcnt lgkmcnt(8)
	v_mfma_f32_32x32x16_bf16 v[80:95], v[184:187], v[120:123], v[80:95]
	v_mfma_f32_32x32x16_bf16 v[64:79], v[188:191], v[120:123], v[64:79]
	ds_read_b128 v[184:187], v223 offset:32768
	ds_read_b128 v[188:191], v223 offset:36864
	s_waitcnt lgkmcnt(8)
	v_mfma_f32_32x32x16_bf16 v[80:95], v[192:195], v[96:99], v[80:95]
	v_mfma_f32_32x32x16_bf16 v[64:79], v[196:199], v[96:99], v[64:79]
	s_waitcnt lgkmcnt(6)
	v_mfma_f32_32x32x16_bf16 v[80:95], v[200:203], v[128:131], v[80:95]
	v_mfma_f32_32x32x16_bf16 v[64:79], v[204:207], v[128:131], v[64:79]
	s_waitcnt lgkmcnt(4)
	v_mfma_f32_32x32x16_bf16 v[80:95], v[208:211], v[136:139], v[80:95]
	v_mfma_f32_32x32x16_bf16 v[64:79], v[212:215], v[136:139], v[64:79]
	s_waitcnt lgkmcnt(2)
	v_mfma_f32_32x32x16_bf16 v[80:95], v[176:179], v[132:135], v[80:95]
	v_mfma_f32_32x32x16_bf16 v[64:79], v[180:183], v[132:135], v[64:79]
	s_waitcnt lgkmcnt(0)
	v_mfma_f32_32x32x16_bf16 v[80:95], v[184:187], v[140:143], v[80:95]
	v_mfma_f32_32x32x16_bf16 v[64:79], v[188:191], v[140:143], v[64:79]
	v_add_u32_e32 v252, s72, v171
	ds_read_b64_tr_b16 v[224:225], v252 offset:0
	ds_read_b64_tr_b16 v[226:227], v252 offset:2048
	ds_read_b64_tr_b16 v[228:229], v252 offset:4096
	ds_read_b64_tr_b16 v[230:231], v252 offset:6144
	ds_read_b64_tr_b16 v[232:233], v252 offset:8192
	ds_read_b64_tr_b16 v[234:235], v252 offset:10240
	ds_read_b64_tr_b16 v[236:237], v252 offset:12288
	ds_read_b64_tr_b16 v[238:239], v252 offset:14336
	s_cbranch_scc1 .LBB0_723
; __device__ __forceinline__ void mask_tile(f32x16& p0, f32x16& p1, int dq) {
;     const float NEG = -__builtin_inff();
; #pragma unroll
;     for (int r = 0; r < 16; ++r) { const int c = (r & 3) + 8 * (r >> 2);
;         if (dq - c < 0) p0[r] = NEG;
;         if (dq - c - 32 < 0) p1[r] = NEG; }
; }
	v_cmp_gt_i32_e64 s[62:63], 26, v172
	v_cmp_gt_i32_e64 s[64:65], 27, v172
	v_cmp_gt_i32_e64 s[60:61], 25, v172
	s_and_b64 s[62:63], s[64:65], s[62:63]
	v_cmp_gt_i32_e64 s[58:59], 24, v172
	s_and_b64 s[60:61], s[62:63], s[60:61]
	v_cmp_gt_i32_e64 s[56:57], 19, v172
	s_and_b64 s[58:59], s[60:61], s[58:59]
	v_cmp_gt_i32_e64 s[54:55], 18, v172
	s_and_b64 s[56:57], s[58:59], s[56:57]
	v_cmp_gt_i32_e64 s[52:53], 17, v172
	s_and_b64 s[54:55], s[56:57], s[54:55]
	v_cmp_gt_i32_e64 s[50:51], 16, v172
	s_and_b64 s[52:53], s[54:55], s[52:53]
	v_cmp_gt_i32_e64 s[48:49], 11, v172
	s_and_b64 s[50:51], s[52:53], s[50:51]
	v_cmp_gt_i32_e64 s[46:47], 10, v172
	s_and_b64 s[48:49], s[50:51], s[48:49]
	v_cmp_gt_i32_e64 s[44:45], 9, v172
	s_and_b64 s[46:47], s[48:49], s[46:47]
	v_cmp_gt_i32_e64 s[42:43], 8, v172
	s_and_b64 s[44:45], s[46:47], s[44:45]
	v_cmp_gt_i32_e64 s[40:41], 3, v172
	s_and_b64 s[42:43], s[44:45], s[42:43]
	v_cmp_gt_i32_e64 s[38:39], 2, v172
	s_and_b64 s[40:41], s[42:43], s[40:41]
	v_cmp_gt_i32_e64 s[36:37], 1, v172
	s_and_b64 s[38:39], s[40:41], s[38:39]
	v_cmp_gt_i32_e64 s[34:35], 0, v172
	s_and_b64 s[36:37], s[38:39], s[36:37]
	s_and_b64 s[34:35], s[36:37], s[34:35]
	v_cmp_gt_i32_e64 s[30:31], 58, v172
	v_cndmask_b32_e64 v80, v80, v173, s[34:35]
	v_cmp_gt_i32_e64 s[34:35], 59, v172
	v_cmp_gt_i32_e64 s[28:29], 57, v172
	s_and_b64 s[30:31], s[34:35], s[30:31]
	v_cmp_gt_i32_e64 s[26:27], 56, v172
	s_and_b64 s[28:29], s[30:31], s[28:29]
	v_cmp_gt_i32_e64 s[24:25], 51, v172
	s_and_b64 s[26:27], s[28:29], s[26:27]
	v_cmp_gt_i32_e64 s[22:23], 50, v172
	s_and_b64 s[24:25], s[26:27], s[24:25]
	v_cmp_gt_i32_e64 s[20:21], 49, v172
	s_and_b64 s[22:23], s[24:25], s[22:23]
	v_cmp_gt_i32_e64 s[18:19], 48, v172
	s_and_b64 s[20:21], s[22:23], s[20:21]
	v_cmp_gt_i32_e64 s[16:17], 43, v172
	s_and_b64 s[18:19], s[20:21], s[18:19]
	v_cmp_gt_i32_e64 s[14:15], 42, v172
	s_and_b64 s[16:17], s[18:19], s[16:17]
	v_cmp_gt_i32_e64 s[12:13], 41, v172
	s_and_b64 s[14:15], s[16:17], s[14:15]
	v_cmp_gt_i32_e64 s[10:11], 40, v172
	s_and_b64 s[12:13], s[14:15], s[12:13]
	v_cmp_gt_i32_e64 s[8:9], 35, v172
	s_and_b64 s[10:11], s[12:13], s[10:11]
	v_cmp_gt_i32_e64 s[6:7], 34, v172
	s_and_b64 s[8:9], s[10:11], s[8:9]
	v_cmp_gt_i32_e64 s[4:5], 33, v172
	v_cndmask_b32_e64 v94, v94, v173, s[62:63]
	v_cndmask_b32_e64 v93, v93, v173, s[60:61]
	v_cndmask_b32_e64 v92, v92, v173, s[58:59]
	v_cndmask_b32_e64 v91, v91, v173, s[56:57]
	v_cndmask_b32_e64 v90, v90, v173, s[54:55]
	v_cndmask_b32_e64 v89, v89, v173, s[52:53]
	v_cndmask_b32_e64 v88, v88, v173, s[50:51]
	v_cndmask_b32_e64 v87, v87, v173, s[48:49]
	v_readlane_b32 s48, v254, 42
	s_and_b64 s[6:7], s[8:9], s[6:7]
	v_cmp_gt_i32_e32 vcc, 32, v172
	v_readlane_b32 s52, v254, 46
	v_readlane_b32 s53, v254, 47
	v_readlane_b32 s56, v254, 50
	v_readlane_b32 s57, v254, 51
	v_readlane_b32 s58, v254, 52
	v_readlane_b32 s59, v254, 53
	v_readlane_b32 s60, v254, 54
	v_readlane_b32 s61, v254, 55
	s_and_b64 s[4:5], s[6:7], s[4:5]
	v_readlane_b32 s62, v254, 56
	v_readlane_b32 s63, v254, 57
	s_mov_b64 s[52:53], s[56:57]
	s_mov_b64 s[56:57], s[60:61]
	s_and_b64 vcc, s[4:5], vcc
	v_cndmask_b32_e64 v95, v95, v173, s[64:65]
	s_mov_b64 s[58:59], s[62:63]
	v_cndmask_b32_e64 v86, v86, v173, s[46:47]
	v_cndmask_b32_e64 v85, v85, v173, s[44:45]
	v_cndmask_b32_e64 v84, v84, v173, s[42:43]
	v_cndmask_b32_e64 v83, v83, v173, s[40:41]
	v_cndmask_b32_e64 v82, v82, v173, s[38:39]
	v_cndmask_b32_e64 v81, v81, v173, s[36:37]
	v_cndmask_b32_e64 v79, v79, v173, s[34:35]
	v_cndmask_b32_e64 v78, v78, v173, s[30:31]
	v_cndmask_b32_e64 v77, v77, v173, s[28:29]
	v_cndmask_b32_e64 v76, v76, v173, s[26:27]
	v_cndmask_b32_e64 v75, v75, v173, s[24:25]
	v_cndmask_b32_e64 v74, v74, v173, s[22:23]
	v_cndmask_b32_e64 v73, v73, v173, s[20:21]
	v_cndmask_b32_e64 v72, v72, v173, s[18:19]
	v_cndmask_b32_e64 v71, v71, v173, s[16:17]
	v_cndmask_b32_e64 v70, v70, v173, s[14:15]
	v_cndmask_b32_e64 v69, v69, v173, s[12:13]
	v_cndmask_b32_e64 v68, v68, v173, s[10:11]
	v_cndmask_b32_e64 v67, v67, v173, s[8:9]
	v_cndmask_b32_e64 v66, v66, v173, s[6:7]
	v_cndmask_b32_e64 v65, v65, v173, s[4:5]
	v_cndmask_b32_e32 v64, v64, v173, vcc
	v_readlane_b32 s49, v254, 43
	v_readlane_b32 s50, v254, 44
	v_readlane_b32 s51, v254, 45
	v_readlane_b32 s54, v254, 48
	v_readlane_b32 s55, v254, 49

; #define LAS __attribute__((address_space(3)))
; __device__ __forceinline__ void partialSM(f32x16& p0, f32x16& p1, float& m_reg, float& mn, float& alpha) {
;     ...
;     mn = fmaxf(m_reg, pmax); alpha = __builtin_amdgcn_exp2f((m_reg - mn) * C2); m_reg = mn;
;     const float mnL = -mn * C2;
; #pragma unroll
;     for (int r = 0; r < 16; ++r) p0[r] = __builtin_amdgcn_exp2f(fmaf(p0[r], C2, mnL));
; #pragma unroll
;     for (int r = 0; r < 16; ++r) p1[r] = __builtin_amdgcn_exp2f(fmaf(p1[r], C2, mnL));
; }
; __device__ __forceinline__ void finishSM(f32x16& p0, f32x16& p1, float alpha, float& l_reg, bf16x8& pa0, bf16x8& pa1, bf16x8& pa2, bf16x8& pa3) {
;     float ps = 0;
; #pragma unroll
;     for (int r = 0; r < 16; ++r) ps += p0[r];
; #pragma unroll
;     for (int r = 0; r < 16; ++r) ps += p1[r];
;     { auto rr = __builtin_amdgcn_permlane32_swap(__float_as_uint(ps), __float_as_uint(ps), false, false);
;       ps = __uint_as_float(rr[0]) + __uint_as_float(rr[1]); }
;     l_reg = l_reg * alpha + ps;
;     ...
;     PK4(p0, 0, pa0); PK4(p0, 8, pa1); PK4(p1, 0, pa2); PK4(p1, 8, pa3);
;     ...
; }
; __device__ __forceinline__ void qkt(f32x16& p0, f32x16& p1, LAS unsigned char* lds  , int r32, int hi, const bf16x8* qr) {
;     p0 = f32x16{}; p1 = f32x16{};
;     const LAS unsigned char* kb[4];
; #pragma unroll
;     for (int dd = 0; dd < 4; ++dd) kb[dd] = lds + K_OFF + KSWZ(r32, (dd * 16 + hi * 8) * 2);
; #pragma unroll
;     for (int d0 = 0; d0 < 8; ++d0) { const LAS unsigned char* a = kb[d0 & 3] + (d0 >> 2) * 128;
;         const bf16x8 b0 = *(const LAS bf16x8*)(a);
;         const bf16x8 b1 = *(const LAS bf16x8*)(a + 32 * 256);
;         p0 = __builtin_amdgcn_mfma_f32_32x32x16_bf16(b0, qr[d0], p0, 0, 0, 0);
;         p1 = __builtin_amdgcn_mfma_f32_32x32x16_bf16(b1, qr[d0], p1, 0, 0, 0); }
; #pragma unroll
;     for (int e = 0; e < 4; ++e) { const LAS unsigned char* a = lds + P_OFF + KPSWZ(r32, (e * 2 + hi) * 16);
;         const bf16x8 b0 = *(const LAS bf16x8*)(a);
;         const bf16x8 b1 = *(const LAS bf16x8*)(a + 32 * 128);
;         p0 = __builtin_amdgcn_mfma_f32_32x32x16_bf16(b0, qr[8 + e], p0, 0, 0, 0);
;         p1 = __builtin_amdgcn_mfma_f32_32x32x16_bf16(b1, qr[8 + e], p1, 0, 0, 0); }
; }
; __device__ __forceinline__ void pv_tile(f32x16* o, int vb0  , bf16x8 pa0, bf16x8 pa1, bf16x8 pa2, bf16x8 pa3) {
;     ...
;     PV_D0(0); PV_D0(1); PV_D0(2); PV_D0(3);
.LBB0_727:
	v_mul_f32_e32 v176, 0xbdd53b94, v174
	v_fmamk_f32 v64, v64, 0x3dd53b94, v176
	v_exp_f32_e32 v177, v64
	v_fmamk_f32 v64, v65, 0x3dd53b94, v176
	v_exp_f32_e32 v178, v64
	v_fmamk_f32 v64, v66, 0x3dd53b94, v176
	v_exp_f32_e32 v179, v64
	v_fmamk_f32 v64, v67, 0x3dd53b94, v176
	v_exp_f32_e32 v180, v64
	v_fmamk_f32 v64, v68, 0x3dd53b94, v176
	v_exp_f32_e32 v181, v64
	v_fmamk_f32 v64, v69, 0x3dd53b94, v176
	v_exp_f32_e32 v182, v64
	v_fmamk_f32 v64, v70, 0x3dd53b94, v176
	v_exp_f32_e32 v183, v64
	v_fmamk_f32 v64, v71, 0x3dd53b94, v176
	v_exp_f32_e32 v184, v64
	v_fmamk_f32 v64, v72, 0x3dd53b94, v176
	v_exp_f32_e32 v185, v64
	v_fmamk_f32 v64, v73, 0x3dd53b94, v176
	v_fmamk_f32 v80, v80, 0x3dd53b94, v176
	v_exp_f32_e32 v186, v64
	v_fmamk_f32 v64, v74, 0x3dd53b94, v176
	v_exp_f32_e32 v80, v80
	v_fmamk_f32 v81, v81, 0x3dd53b94, v176
	v_exp_f32_e32 v187, v64
	v_fmamk_f32 v64, v75, 0x3dd53b94, v176
	v_exp_f32_e32 v81, v81
	v_fmamk_f32 v82, v82, 0x3dd53b94, v176
	v_exp_f32_e32 v188, v64
	v_fmamk_f32 v64, v76, 0x3dd53b94, v176
	v_exp_f32_e32 v82, v82
	v_fmamk_f32 v83, v83, 0x3dd53b94, v176
	v_exp_f32_e32 v189, v64
	v_fmamk_f32 v64, v77, 0x3dd53b94, v176
	v_exp_f32_e32 v83, v83
	v_fmamk_f32 v84, v84, 0x3dd53b94, v176
	v_exp_f32_e32 v190, v64
	v_fmamk_f32 v64, v78, 0x3dd53b94, v176
	v_exp_f32_e32 v84, v84
	v_fmamk_f32 v85, v85, 0x3dd53b94, v176
	v_exp_f32_e32 v191, v64
	v_add_f32_e32 v64, 0, v80
	v_exp_f32_e32 v85, v85
	v_fmamk_f32 v86, v86, 0x3dd53b94, v176
	v_add_f32_e32 v64, v81, v64
	v_exp_f32_e32 v86, v86
	v_fmamk_f32 v87, v87, 0x3dd53b94, v176
	v_add_f32_e32 v64, v82, v64
	v_exp_f32_e32 v87, v87
	v_fmamk_f32 v88, v88, 0x3dd53b94, v176
	v_add_f32_e32 v64, v83, v64
	v_exp_f32_e32 v88, v88
	v_fmamk_f32 v89, v89, 0x3dd53b94, v176
	v_add_f32_e32 v64, v84, v64
	v_exp_f32_e32 v89, v89
	v_fmamk_f32 v90, v90, 0x3dd53b94, v176
	v_add_f32_e32 v64, v85, v64
	v_exp_f32_e32 v90, v90
	v_fmamk_f32 v91, v91, 0x3dd53b94, v176
	v_add_f32_e32 v64, v86, v64
	v_exp_f32_e32 v91, v91
	v_fmamk_f32 v92, v92, 0x3dd53b94, v176
	v_add_f32_e32 v64, v87, v64
	v_exp_f32_e32 v92, v92
	v_fmamk_f32 v93, v93, 0x3dd53b94, v176
	v_add_f32_e32 v64, v88, v64
	v_exp_f32_e32 v93, v93
	v_fmamk_f32 v94, v94, 0x3dd53b94, v176
	v_add_f32_e32 v64, v89, v64
	v_exp_f32_e32 v94, v94
	v_fmamk_f32 v95, v95, 0x3dd53b94, v176
	v_add_f32_e32 v64, v90, v64
	v_exp_f32_e32 v95, v95
	v_add_f32_e32 v64, v91, v64
	v_add_f32_e32 v64, v92, v64
	v_add_f32_e32 v64, v93, v64
	v_add_f32_e32 v64, v94, v64
	v_add_f32_e32 v64, v95, v64
	v_add_f32_e32 v64, v177, v64
	v_add_f32_e32 v64, v178, v64
	v_add_f32_e32 v64, v179, v64
	v_add_f32_e32 v64, v180, v64
	v_add_f32_e32 v64, v181, v64
	v_add_f32_e32 v64, v182, v64
	v_add_f32_e32 v64, v183, v64
	v_add_f32_e32 v64, v184, v64
	v_add_f32_e32 v64, v185, v64
	v_add_f32_e32 v64, v186, v64
	v_fmac_f32_e32 v176, 0x3dd53b94, v79
	v_add_f32_e32 v64, v187, v64
	v_exp_f32_e32 v79, v176
	v_add_f32_e32 v64, v188, v64
	v_add_f32_e32 v64, v189, v64
	v_add_f32_e32 v64, v190, v64
	v_add_f32_e32 v64, v191, v64
	v_add_f32_e32 v64, v79, v64
	v_mov_b32_e32 v65, v64
	s_nop 1
	v_permlane32_swap_b32_e32 v64, v65
	v_add_f32_e32 v192, v64, v65
	v_cvt_pk_bf16_f32 v64, v80, v81
	v_cvt_pk_bf16_f32 v65, v82, v83
	v_cvt_pk_bf16_f32 v66, v84, v85
	v_cvt_pk_bf16_f32 v67, v86, v87
	v_cvt_pk_bf16_f32 v68, v88, v89
	v_cvt_pk_bf16_f32 v69, v90, v91
	v_cvt_pk_bf16_f32 v70, v92, v93
	v_cvt_pk_bf16_f32 v71, v94, v95
	v_cvt_pk_bf16_f32 v72, v177, v178
	v_cvt_pk_bf16_f32 v73, v179, v180
	v_cvt_pk_bf16_f32 v74, v181, v182
	v_cvt_pk_bf16_f32 v75, v183, v184
	v_cvt_pk_bf16_f32 v76, v185, v186
	v_cvt_pk_bf16_f32 v77, v187, v188
	v_cvt_pk_bf16_f32 v78, v189, v190
	v_cvt_pk_bf16_f32 v79, v191, v79
	v_fmac_f32_e32 v192, v145, v175
	v_permlane32_swap_b32_e32 v64, v66
	v_permlane32_swap_b32_e32 v65, v67
	v_permlane32_swap_b32_e32 v68, v70
	v_permlane32_swap_b32_e32 v69, v71
	v_permlane32_swap_b32_e32 v72, v74
	v_permlane32_swap_b32_e32 v73, v75
	v_permlane32_swap_b32_e32 v76, v78
	v_permlane32_swap_b32_e32 v77, v79
	ds_read_b64_tr_b16 v[80:81], v252 offset:512
	ds_read_b64_tr_b16 v[82:83], v252 offset:2560
	ds_read_b64_tr_b16 v[84:85], v252 offset:4608
	ds_read_b64_tr_b16 v[86:87], v252 offset:6656
	ds_read_b64_tr_b16 v[88:89], v252 offset:8704
	ds_read_b64_tr_b16 v[90:91], v252 offset:10752
	ds_read_b64_tr_b16 v[92:93], v252 offset:12800
	ds_read_b64_tr_b16 v[94:95], v252 offset:14848
	s_waitcnt lgkmcnt(8)
	v_mfma_f32_32x32x16_bf16 v[48:63], v[64:67], v[224:227], v[48:63]
	v_mfma_f32_32x32x16_bf16 v[48:63], v[68:71], v[228:231], v[48:63]
	v_mfma_f32_32x32x16_bf16 v[48:63], v[72:75], v[232:235], v[48:63]
	v_mfma_f32_32x32x16_bf16 v[48:63], v[76:79], v[236:239], v[48:63]
	ds_read_b64_tr_b16 v[224:225], v252 offset:1024
	ds_read_b64_tr_b16 v[226:227], v252 offset:3072
	ds_read_b64_tr_b16 v[228:229], v252 offset:5120
	ds_read_b64_tr_b16 v[230:231], v252 offset:7168
	ds_read_b64_tr_b16 v[232:233], v252 offset:9216
	ds_read_b64_tr_b16 v[234:235], v252 offset:11264
	ds_read_b64_tr_b16 v[236:237], v252 offset:13312
	ds_read_b64_tr_b16 v[238:239], v252 offset:15360
	s_waitcnt lgkmcnt(8)
	v_mfma_f32_32x32x16_bf16 v[32:47], v[64:67], v[80:83], v[32:47]
	v_mfma_f32_32x32x16_bf16 v[32:47], v[68:71], v[84:87], v[32:47]
	v_mfma_f32_32x32x16_bf16 v[32:47], v[72:75], v[88:91], v[32:47]
	v_mfma_f32_32x32x16_bf16 v[32:47], v[76:79], v[92:95], v[32:47]
	ds_read_b64_tr_b16 v[80:81], v252 offset:1536
	ds_read_b64_tr_b16 v[82:83], v252 offset:3584
	ds_read_b64_tr_b16 v[84:85], v252 offset:5632
	ds_read_b64_tr_b16 v[86:87], v252 offset:7680
	ds_read_b64_tr_b16 v[88:89], v252 offset:9728
	ds_read_b64_tr_b16 v[90:91], v252 offset:11776
	ds_read_b64_tr_b16 v[92:93], v252 offset:13824
	ds_read_b64_tr_b16 v[94:95], v252 offset:15872
	s_waitcnt lgkmcnt(8)
	v_mfma_f32_32x32x16_bf16 v[16:31], v[64:67], v[224:227], v[16:31]
	v_mfma_f32_32x32x16_bf16 v[16:31], v[68:71], v[228:231], v[16:31]
	v_mfma_f32_32x32x16_bf16 v[16:31], v[72:75], v[232:235], v[16:31]
	v_mfma_f32_32x32x16_bf16 v[16:31], v[76:79], v[236:239], v[16:31]
	s_waitcnt lgkmcnt(0)
	v_mov_b32_e32 v145, v192
	v_mfma_f32_32x32x16_bf16 v[0:15], v[64:67], v[80:83], v[0:15]
	v_mfma_f32_32x32x16_bf16 v[0:15], v[68:71], v[84:87], v[0:15]
	v_mfma_f32_32x32x16_bf16 v[0:15], v[72:75], v[88:91], v[0:15]
	v_mfma_f32_32x32x16_bf16 v[0:15], v[76:79], v[92:95], v[0:15]
	s_branch .LBB0_729
